# v24 with the tile j+2 LDS-DMA issue moved from behind the tile barrier into the gap between sub-head-0 softmax and sub-head-1 scores (replaces the idle spacer) in both diff-attention loops
# speedup vs baseline: 1.0048x; 1.0048x over previous
.LBB0_186:
.LBB0_187:
	s_cmp_eq_u32 s71, 0
	s_cbranch_scc1 .LBB0_189

.LBB0_195:
	v_add_u32_e32 v0, s49, v225
	v_add_u32_e32 v6, v0, v227
	v_add_u32_e32 v7, v0, v228
	ds_read_b128 v[244:247], v6
	ds_read_b128 v[248:251], v6 offset:8192
	ds_read_b128 v[236:239], v7
	ds_read_b128 v[208:211], v7 offset:8192
	v_add_u32_e32 v6, v0, v229
	v_add_u32_e32 v7, v0, v230
	ds_read_b128 v[2:5], v6
	ds_read_b128 v[8:11], v6 offset:8192
	ds_read_b128 v[12:15], v7
	s_xor_b64 s[44:45], s[44:45], -1
	v_add_u32_e32 v6, v0, v226
	s_waitcnt lgkmcnt(6)
	v_mfma_f32_32x32x16_bf16 v[144:159], v[244:247], v[176:179], v[144:159]
	ds_read_b128 v[244:247], v7 offset:8192
	s_waitcnt lgkmcnt(6)
	v_mfma_f32_32x32x16_bf16 v[160:175], v[248:251], v[176:179], v[160:175]
	s_waitcnt lgkmcnt(5)
	v_mfma_f32_32x32x16_bf16 v[144:159], v[236:239], v[180:183], v[144:159]
	ds_read_b128 v[248:251], v6
	ds_read_b128 v[236:239], v6 offset:8192
	s_waitcnt lgkmcnt(6)
	v_mfma_f32_32x32x16_bf16 v[160:175], v[208:211], v[180:183], v[160:175]
	v_add_u32_e32 v7, v0, v231
	s_waitcnt lgkmcnt(5)
	v_mfma_f32_32x32x16_bf16 v[144:159], v[2:5], v[184:187], v[144:159]
	s_waitcnt lgkmcnt(4)
	v_mfma_f32_32x32x16_bf16 v[160:175], v[8:11], v[184:187], v[160:175]
	s_waitcnt lgkmcnt(3)
	v_mfma_f32_32x32x16_bf16 v[144:159], v[12:15], v[188:191], v[144:159]
	s_waitcnt lgkmcnt(2)
	v_mfma_f32_32x32x16_bf16 v[160:175], v[244:247], v[188:191], v[160:175]
	ds_read_b128 v[244:247], v7
	s_nop 9
	v_exp_f32_e32 v6, v144
	v_exp_f32_e32 v3, v145
	v_exp_f32_e32 v10, v148
	v_exp_f32_e32 v11, v149
	v_exp_f32_e32 v12, v150
	v_exp_f32_e32 v148, v152
	v_exp_f32_e32 v150, v153
	v_exp_f32_e32 v156, v156
	v_exp_f32_e32 v157, v157
	v_exp_f32_e32 v5, v146
	v_exp_f32_e32 v152, v154
	v_exp_f32_e32 v158, v158
	v_exp_f32_e32 v8, v147
	v_exp_f32_e32 v13, v151
	v_exp_f32_e32 v154, v155
	v_exp_f32_e32 v159, v159
	v_exp_f32_e32 v2, v160
	v_exp_f32_e32 v144, v164
	v_exp_f32_e32 v149, v168
	v_exp_f32_e32 v160, v172
	v_exp_f32_e32 v4, v161
	v_exp_f32_e32 v145, v165
	v_exp_f32_e32 v151, v169
	v_exp_f32_e32 v161, v173
	v_add_f32_e32 v14, v6, v3
	v_add_f32_e32 v15, v10, v11
	v_add_f32_e32 v164, v148, v150
	v_add_f32_e32 v165, v156, v157
	v_exp_f32_e32 v7, v162
	v_exp_f32_e32 v146, v166
	v_exp_f32_e32 v153, v170
	v_exp_f32_e32 v162, v174
	v_add_f32_e32 v14, v5, v14
	v_add_f32_e32 v15, v12, v15
	v_add_f32_e32 v164, v152, v164
	v_add_f32_e32 v165, v158, v165
	v_exp_f32_e32 v9, v163
	v_exp_f32_e32 v147, v167
	v_exp_f32_e32 v155, v171
	v_exp_f32_e32 v163, v175
	v_add_f32_e32 v14, v8, v14
	v_add_f32_e32 v15, v13, v15
	v_add_f32_e32 v164, v154, v164
	v_add_f32_e32 v165, v159, v165
	v_add_f32_e32 v14, v2, v14
	v_add_f32_e32 v15, v144, v15
	v_add_f32_e32 v164, v149, v164
	v_add_f32_e32 v165, v160, v165
	v_add_f32_e32 v14, v4, v14
	v_add_f32_e32 v15, v145, v15
	v_add_f32_e32 v164, v151, v164
	v_add_f32_e32 v165, v161, v165
	v_add_f32_e32 v14, v7, v14
	v_add_f32_e32 v15, v146, v15
	v_add_f32_e32 v164, v153, v164
	v_add_f32_e32 v165, v162, v165
	v_add_f32_e32 v14, v9, v14
	v_add_f32_e32 v15, v147, v15
	v_add_f32_e32 v164, v155, v164
	v_add_f32_e32 v165, v163, v165
	v_add_f32_e32 v14, v14, v15
	v_add_f32_e32 v15, v164, v165
	v_add_f32_e32 v14, v14, v15
	v_mov_b32_e32 v15, v14
	v_cvt_pk_bf16_f32 v208, v6, v3
	v_cvt_pk_bf16_f32 v209, v5, v8
	v_cvt_pk_bf16_f32 v210, v10, v11
	v_cvt_pk_bf16_f32 v211, v12, v13
	v_cvt_pk_bf16_f32 v10, v148, v150
	v_cvt_pk_bf16_f32 v11, v152, v154
	v_cvt_pk_bf16_f32 v12, v156, v157
	v_cvt_pk_bf16_f32 v13, v158, v159
	v_cvt_pk_bf16_f32 v6, v2, v4
	v_cvt_pk_bf16_f32 v7, v7, v9
	v_cvt_pk_bf16_f32 v8, v144, v145
	v_cvt_pk_bf16_f32 v9, v146, v147
	v_cvt_pk_bf16_f32 v2, v149, v151
	v_cvt_pk_bf16_f32 v3, v153, v155
	v_cvt_pk_bf16_f32 v4, v160, v161
	v_cvt_pk_bf16_f32 v5, v162, v163
	v_permlane32_swap_b32_e32 v14, v15
	v_permlane32_swap_b32_e32 v208, v210
	v_permlane32_swap_b32_e32 v209, v211
	v_permlane32_swap_b32_e32 v10, v12
	v_permlane32_swap_b32_e32 v11, v13
	v_permlane32_swap_b32_e32 v6, v8
	v_permlane32_swap_b32_e32 v7, v9
	v_permlane32_swap_b32_e32 v2, v4
	v_permlane32_swap_b32_e32 v3, v5
	s_cmp_gt_u32 s86, 61
	s_cbranch_scc1 .Ldmxb
	s_add_i32 s32, s7, s90
	v_lshl_add_u64 v[252:253], s[40:41], 0, v[218:219]
	s_mov_b32 m0, s32
	s_nop 0
	global_load_lds_dwordx4 v[252:253], off
	v_lshl_add_u64 v[252:253], s[40:41], 0, v[214:215]
	s_add_i32 m0, s32, 0x400
	s_add_i32 s32, s3, s90
	global_load_lds_dwordx4 v[252:253], off
	v_lshl_add_u64 v[252:253], s[40:41], 0, v[216:217]
	v_lshl_add_u64 v[252:253], v[252:253], 0, s[24:25]
	s_mov_b32 m0, s32
	s_nop 0
	global_load_lds_dwordx4 v[252:253], off
	v_lshl_add_u64 v[252:253], s[40:41], 0, v[216:217]
	v_lshl_add_u64 v[252:253], v[252:253], 0, s[26:27]
	s_add_i32 m0, s32, 0x400
	s_nop 0
	global_load_lds_dwordx4 v[252:253], off
.Ldmxb:
	v_mov_b32_e32 v160, 0
	s_andn2_b64 vcc, exec, s[44:45]
	v_mov_b32_e32 v161, 0
	v_mov_b32_e32 v162, 0
	v_mov_b32_e32 v163, 0
	v_mov_b32_e32 v164, 0
	v_mov_b32_e32 v165, 0
	v_mov_b32_e32 v166, 0
	v_mov_b32_e32 v167, 0
	v_mov_b32_e32 v168, 0
	v_mov_b32_e32 v169, 0
	v_mov_b32_e32 v170, 0
	v_mov_b32_e32 v171, 0
	v_mov_b32_e32 v172, 0
	v_mov_b32_e32 v173, 0
	v_mov_b32_e32 v174, 0
	v_mov_b32_e32 v175, 0
	v_mov_b32_e32 v144, 0
	v_mov_b32_e32 v145, 0
	v_mov_b32_e32 v146, 0
	v_mov_b32_e32 v147, 0
	v_mov_b32_e32 v148, 0
	v_mov_b32_e32 v149, 0
	v_mov_b32_e32 v150, 0
	v_mov_b32_e32 v151, 0
	v_mov_b32_e32 v152, 0
	v_mov_b32_e32 v153, 0
	v_mov_b32_e32 v154, 0
	v_mov_b32_e32 v155, 0
	v_mov_b32_e32 v156, 0
	v_mov_b32_e32 v157, 0
	v_mov_b32_e32 v158, 0
	v_mov_b32_e32 v159, 0
	s_cbranch_vccnz .LBB0_200
	s_andn2_b64 vcc, exec, s[42:43]
	s_mov_b64 s[42:43], -1
	s_cbranch_vccnz .LBB0_198
	v_add_u32_e32 v144, 0x21780, v212
	v_add_u32_e32 v146, 0x21708, v212
	v_add_u32_e32 v147, 0x21788, v212
	v_add_u32_e32 v148, 0x21720, v212
	v_add_u32_e32 v149, 0x217a0, v212
	v_add_u32_e32 v150, 0x21728, v212
	v_add_u32_e32 v151, 0x217a8, v212
	v_add_u32_e32 v152, 0x21740, v212
	v_add_u32_e32 v153, 0x217c0, v212
	v_add_u32_e32 v154, 0x21748, v212
	v_add_u32_e32 v155, 0x217c8, v212
	v_add_u32_e32 v156, 0x21760, v212
	v_add_u32_e32 v157, 0x217e0, v212
	v_add_u32_e32 v158, 0x21768, v212
	v_add_u32_e32 v159, 0x217e8, v212
	ds_read2_b32 v[160:161], v213 offset1:1
	ds_read2_b32 v[144:145], v144 offset1:1
	ds_read2_b32 v[162:163], v146 offset1:1
	ds_read2_b32 v[146:147], v147 offset1:1
	ds_read2_b32 v[164:165], v148 offset1:1
	ds_read2_b32 v[148:149], v149 offset1:1
	ds_read2_b32 v[166:167], v150 offset1:1
	ds_read2_b32 v[150:151], v151 offset1:1
	ds_read2_b32 v[168:169], v152 offset1:1
	ds_read2_b32 v[152:153], v153 offset1:1
	ds_read2_b32 v[170:171], v154 offset1:1
	ds_read2_b32 v[154:155], v155 offset1:1
	ds_read2_b32 v[172:173], v156 offset1:1
	ds_read2_b32 v[156:157], v157 offset1:1
	ds_read2_b32 v[174:175], v158 offset1:1
	ds_read2_b32 v[158:159], v159 offset1:1
	s_mov_b64 s[42:43], 0

.LBB0_215:
	v_add_u32_e32 v212, s56, v225
	v_add_u32_e32 v6, v212, v227
	v_add_u32_e32 v7, v212, v228
	ds_read_b128 v[244:247], v6
	ds_read_b128 v[248:251], v6 offset:8192
	ds_read_b128 v[236:239], v7
	ds_read_b128 v[240:243], v7 offset:8192
	v_add_u32_e32 v6, v212, v229
	v_add_u32_e32 v7, v212, v230
	ds_read_b128 v[2:5], v6
	ds_read_b128 v[8:11], v6 offset:8192
	ds_read_b128 v[208:211], v7
	s_xor_b64 s[44:45], s[44:45], -1
	v_add_u32_e32 v6, v212, v226
	s_waitcnt lgkmcnt(6)
	v_mfma_f32_32x32x16_bf16 v[160:175], v[244:247], v[176:179], v[160:175]
	ds_read_b128 v[244:247], v7 offset:8192
	s_waitcnt lgkmcnt(6)
	v_mfma_f32_32x32x16_bf16 v[144:159], v[248:251], v[176:179], v[144:159]
	s_waitcnt lgkmcnt(5)
	v_mfma_f32_32x32x16_bf16 v[160:175], v[236:239], v[180:183], v[160:175]
	v_add_u32_e32 v7, v212, v231
	s_waitcnt lgkmcnt(4)
	v_mfma_f32_32x32x16_bf16 v[144:159], v[240:243], v[180:183], v[144:159]
	ds_read_b128 v[248:251], v6
	ds_read_b128 v[236:239], v6 offset:8192
	ds_read_b128 v[240:243], v7
	s_waitcnt lgkmcnt(6)
	v_mfma_f32_32x32x16_bf16 v[160:175], v[2:5], v[184:187], v[160:175]
	s_waitcnt lgkmcnt(5)
	v_mfma_f32_32x32x16_bf16 v[144:159], v[8:11], v[184:187], v[144:159]
	s_waitcnt lgkmcnt(4)
	v_mfma_f32_32x32x16_bf16 v[160:175], v[208:211], v[188:191], v[160:175]
	s_waitcnt lgkmcnt(3)
	v_mfma_f32_32x32x16_bf16 v[144:159], v[244:247], v[188:191], v[144:159]
	ds_read_b128 v[244:247], v7 offset:8192
	s_nop 9
	v_exp_f32_e32 v6, v160
	v_exp_f32_e32 v3, v161
	v_exp_f32_e32 v10, v164
	v_exp_f32_e32 v11, v165
	v_exp_f32_e32 v160, v172
	v_exp_f32_e32 v161, v173
	v_exp_f32_e32 v5, v162
	v_exp_f32_e32 v2, v144
	v_exp_f32_e32 v7, v146
	v_exp_f32_e32 v144, v148
	v_exp_f32_e32 v146, v150
	v_exp_f32_e32 v148, v168
	v_exp_f32_e32 v150, v169
	v_exp_f32_e32 v4, v145
	v_exp_f32_e32 v145, v149
	v_exp_f32_e32 v12, v166
	v_exp_f32_e32 v149, v152
	v_exp_f32_e32 v152, v170
	v_exp_f32_e32 v162, v174
	v_exp_f32_e32 v8, v163
	v_exp_f32_e32 v9, v147
	v_exp_f32_e32 v13, v167
	v_exp_f32_e32 v147, v151
	v_exp_f32_e32 v151, v153
	v_exp_f32_e32 v153, v154
	v_exp_f32_e32 v154, v171
	v_exp_f32_e32 v163, v175
	v_exp_f32_e32 v156, v156
	v_exp_f32_e32 v157, v157
	v_add_f32_e32 v164, v6, v3
	v_add_f32_e32 v165, v10, v11
	v_add_f32_e32 v166, v148, v150
	v_add_f32_e32 v167, v160, v161
	v_exp_f32_e32 v158, v158
	v_add_f32_e32 v164, v5, v164
	v_add_f32_e32 v165, v12, v165
	v_add_f32_e32 v166, v152, v166
	v_add_f32_e32 v167, v162, v167
	v_exp_f32_e32 v155, v155
	v_exp_f32_e32 v159, v159
	v_add_f32_e32 v164, v8, v164
	v_add_f32_e32 v165, v13, v165
	v_add_f32_e32 v166, v154, v166
	v_add_f32_e32 v167, v163, v167
	v_add_f32_e32 v164, v2, v164
	v_add_f32_e32 v165, v144, v165
	v_add_f32_e32 v166, v149, v166
	v_add_f32_e32 v167, v156, v167
	v_add_f32_e32 v164, v4, v164
	v_add_f32_e32 v165, v145, v165
	v_add_f32_e32 v166, v151, v166
	v_add_f32_e32 v167, v157, v167
	v_add_f32_e32 v164, v7, v164
	v_add_f32_e32 v165, v146, v165
	v_add_f32_e32 v166, v153, v166
	v_add_f32_e32 v167, v158, v167
	v_add_f32_e32 v164, v9, v164
	v_add_f32_e32 v165, v147, v165
	v_add_f32_e32 v166, v155, v166
	v_add_f32_e32 v167, v159, v167
	v_add_f32_e32 v164, v164, v165
	v_add_f32_e32 v165, v166, v167
	v_add_f32_e32 v213, v164, v165
	v_mov_b32_e32 v218, v213
	v_cvt_pk_bf16_f32 v208, v6, v3
	v_cvt_pk_bf16_f32 v209, v5, v8
	v_cvt_pk_bf16_f32 v210, v10, v11
	v_cvt_pk_bf16_f32 v211, v12, v13
	v_cvt_pk_bf16_f32 v10, v148, v150
	v_cvt_pk_bf16_f32 v11, v152, v154
	v_cvt_pk_bf16_f32 v12, v160, v161
	v_cvt_pk_bf16_f32 v13, v162, v163
	v_cvt_pk_bf16_f32 v6, v2, v4
	v_cvt_pk_bf16_f32 v7, v7, v9
	v_cvt_pk_bf16_f32 v8, v144, v145
	v_cvt_pk_bf16_f32 v9, v146, v147
	v_cvt_pk_bf16_f32 v2, v149, v151
	v_cvt_pk_bf16_f32 v3, v153, v155
	v_cvt_pk_bf16_f32 v4, v156, v157
	v_cvt_pk_bf16_f32 v5, v158, v159
	v_permlane32_swap_b32_e32 v213, v218
	v_permlane32_swap_b32_e32 v208, v210
	v_permlane32_swap_b32_e32 v209, v211
	v_permlane32_swap_b32_e32 v10, v12
	v_permlane32_swap_b32_e32 v11, v13
	v_permlane32_swap_b32_e32 v6, v8
	v_permlane32_swap_b32_e32 v7, v9
	v_permlane32_swap_b32_e32 v2, v4
	v_permlane32_swap_b32_e32 v3, v5
	s_cmp_gt_u32 s71, 61
	s_cbranch_scc1 .Ldmxa
	s_add_i32 s32, s7, s90
	v_lshl_add_u64 v[252:253], s[40:41], 0, v[216:217]
	s_mov_b32 m0, s32
	s_nop 0
	global_load_lds_dwordx4 v[252:253], off
	v_lshl_add_u64 v[252:253], s[40:41], 0, v[214:215]
	s_add_i32 m0, s32, 0x400
	s_add_i32 s32, s3, s90
	global_load_lds_dwordx4 v[252:253], off
	v_lshl_add_u64 v[252:253], s[40:41], 0, v[14:15]
	v_lshl_add_u64 v[252:253], v[252:253], 0, s[24:25]
	s_mov_b32 m0, s32
	s_nop 0
	global_load_lds_dwordx4 v[252:253], off
	v_lshl_add_u64 v[252:253], s[40:41], 0, v[14:15]
	v_lshl_add_u64 v[252:253], v[252:253], 0, s[26:27]
	s_add_i32 m0, s32, 0x400
	s_nop 0
	global_load_lds_dwordx4 v[252:253], off
.Ldmxa:
	v_mov_b32_e32 v160, 0
	s_andn2_b64 vcc, exec, s[44:45]
	v_mov_b32_e32 v161, 0
	v_mov_b32_e32 v162, 0
	v_mov_b32_e32 v163, 0
	v_mov_b32_e32 v164, 0
	v_mov_b32_e32 v165, 0
	v_mov_b32_e32 v166, 0
	v_mov_b32_e32 v167, 0
	v_mov_b32_e32 v168, 0
	v_mov_b32_e32 v169, 0
	v_mov_b32_e32 v170, 0
	v_mov_b32_e32 v171, 0
	v_mov_b32_e32 v172, 0
	v_mov_b32_e32 v173, 0
	v_mov_b32_e32 v174, 0
	v_mov_b32_e32 v175, 0
	v_mov_b32_e32 v144, 0
	v_mov_b32_e32 v145, 0
	v_mov_b32_e32 v146, 0
	v_mov_b32_e32 v147, 0
	v_mov_b32_e32 v148, 0
	v_mov_b32_e32 v149, 0
	v_mov_b32_e32 v150, 0
	v_mov_b32_e32 v151, 0
	v_mov_b32_e32 v152, 0
	v_mov_b32_e32 v153, 0
	v_mov_b32_e32 v154, 0
	v_mov_b32_e32 v155, 0
	v_mov_b32_e32 v156, 0
	v_mov_b32_e32 v157, 0
	v_mov_b32_e32 v158, 0
	v_mov_b32_e32 v159, 0
	s_cbranch_vccnz .LBB0_205
	s_andn2_b64 vcc, exec, s[42:43]
	s_mov_b64 s[42:43], -1
	s_cbranch_vccnz .LBB0_218
	v_add_u32_e32 v146, 0x21780, v219
	v_add_u32_e32 v147, 0x21708, v219
	v_add_u32_e32 v148, 0x21788, v219
	ds_read2_b32 v[144:145], v220 offset1:1
	ds_read2_b32 v[160:161], v146 offset1:1
	ds_read2_b32 v[146:147], v147 offset1:1
	ds_read2_b32 v[162:163], v148 offset1:1
	v_add_u32_e32 v148, 0x21720, v219
	v_add_u32_e32 v150, 0x217a0, v219
	v_add_u32_e32 v151, 0x21728, v219
	v_add_u32_e32 v152, 0x217a8, v219
	ds_read2_b32 v[148:149], v148 offset1:1
	ds_read2_b32 v[164:165], v150 offset1:1
	ds_read2_b32 v[150:151], v151 offset1:1
	ds_read2_b32 v[166:167], v152 offset1:1
	v_add_u32_e32 v152, 0x21740, v219
	v_add_u32_e32 v154, 0x217c0, v219
	v_add_u32_e32 v155, 0x21748, v219
	v_add_u32_e32 v156, 0x217c8, v219
	ds_read2_b32 v[152:153], v152 offset1:1
	ds_read2_b32 v[168:169], v154 offset1:1
	ds_read2_b32 v[154:155], v155 offset1:1
	ds_read2_b32 v[170:171], v156 offset1:1
	v_add_u32_e32 v156, 0x21760, v219
	v_add_u32_e32 v158, 0x217e0, v219
	v_add_u32_e32 v159, 0x21768, v219
	v_add_u32_e32 v174, 0x217e8, v219
	ds_read2_b32 v[156:157], v156 offset1:1
	ds_read2_b32 v[172:173], v158 offset1:1
	ds_read2_b32 v[158:159], v159 offset1:1
	ds_read2_b32 v[174:175], v174 offset1:1
	s_mov_b64 s[42:43], 0
